# baseline (speedup 1.0000x reference)
.LBB3_11:
	s_lshl_b32 s58, s42, 7
	s_add_i32 s59, s41, 0x400
	s_lshr_b32 s59, s59, 6
	s_bfe_u32 s60, s20, 0x1000c
	s_add_i32 s59, s59, s60
	s_lshl_b32 s59, s59, 19
	s_add_u32 s58, s58, s59
	s_add_u32 s58, s56, s58
	s_addc_u32 s59, s57, 0
	s_add_u32 s60, s58, 0x4000
	s_addc_u32 s61, s59, 0
	s_add_u32 s62, s58, 0x100000
	s_addc_u32 s63, s59, 0
	s_add_u32 s64, s62, 0x4000
	s_addc_u32 s65, s63, 0
	s_lshr_b32 s66, s41, 7
	s_bfe_u32 s67, s20, 0x1000c
	s_add_i32 s66, s66, s67
	s_lshl_b32 s66, s66, 14
	s_lshl_b32 s67, s42, 2
	s_add_u32 s66, s66, s67
	s_add_u32 s66, s14, s66
	s_addc_u32 s67, s15, 0
	v_add_u32_e32 v172, s43, v207
	v_exp_f32_e32 v130, v114
	v_exp_f32_e32 v131, v115
	v_exp_f32_e32 v132, v116
	v_exp_f32_e32 v133, v117
	v_exp_f32_e32 v142, v78
	v_exp_f32_e32 v143, v79
	v_exp_f32_e32 v144, v80
	v_exp_f32_e32 v145, v81
	v_exp_f32_e32 v176, v106
	v_exp_f32_e32 v177, v107
	v_exp_f32_e32 v178, v108
	v_exp_f32_e32 v179, v109
	v_exp_f32_e32 v232, v70
	v_exp_f32_e32 v233, v71
	v_exp_f32_e32 v234, v72
	v_exp_f32_e32 v235, v73
	v_pk_fma_f32 v[130:131], v[130:131], -0.5, -0.5 op_sel_hi:[1,0,0]
	v_pk_fma_f32 v[132:133], v[132:133], -0.5, -0.5 op_sel_hi:[1,0,0]
	v_pk_fma_f32 v[142:143], v[142:143], -0.5, -0.5 op_sel_hi:[1,0,0]
	v_pk_fma_f32 v[144:145], v[144:145], -0.5, -0.5 op_sel_hi:[1,0,0]
	v_pk_fma_f32 v[176:177], v[176:177], -0.5, -0.5 op_sel_hi:[1,0,0]
	v_pk_fma_f32 v[178:179], v[178:179], -0.5, -0.5 op_sel_hi:[1,0,0]
	v_pk_fma_f32 v[232:233], v[232:233], -0.5, -0.5 op_sel_hi:[1,0,0]
	v_pk_fma_f32 v[234:235], v[234:235], -0.5, -0.5 op_sel_hi:[1,0,0]
	v_pk_mul_f32 v[134:135], v[130:131], v[132:133]
	v_pk_mul_f32 v[146:147], v[142:143], v[144:145]
	v_pk_mul_f32 v[180:181], v[176:177], v[178:179]
	v_pk_mul_f32 v[236:237], v[232:233], v[234:235]
	v_rcp_f32_e32 v136, v134
	v_rcp_f32_e32 v137, v135
	v_rcp_f32_e32 v148, v146
	v_rcp_f32_e32 v149, v147
	v_rcp_f32_e32 v182, v180
	v_rcp_f32_e32 v183, v181
	v_rcp_f32_e32 v238, v236
	v_rcp_f32_e32 v239, v237
	v_pk_add_f32 v[164:165], v[114:115], v[116:117]
	v_pk_add_f32 v[164:165], v[164:165], v[78:79]
	v_pk_add_f32 v[164:165], v[164:165], v[80:81]
	v_pk_add_f32 v[164:165], v[164:165], v[106:107]
	v_pk_add_f32 v[164:165], v[164:165], v[108:109]
	v_pk_add_f32 v[164:165], v[164:165], v[70:71]
	v_pk_add_f32 v[164:165], v[164:165], v[72:73]
	v_pk_mul_f32 v[162:163], v[134:135], v[146:147]
	v_pk_mul_f32 v[162:163], v[162:163], v[180:181]
	v_pk_mul_f32 v[162:163], v[162:163], v[236:237]
	v_pk_fma_f32 v[138:139], v[136:137], v[132:133], 1.0 op_sel_hi:[1,1,0]
	v_pk_fma_f32 v[140:141], v[136:137], v[130:131], 1.0 op_sel_hi:[1,1,0]
	v_pk_fma_f32 v[150:151], v[148:149], v[144:145], 1.0 op_sel_hi:[1,1,0]
	v_pk_fma_f32 v[152:153], v[148:149], v[142:143], 1.0 op_sel_hi:[1,1,0]
	v_pk_fma_f32 v[184:185], v[182:183], v[178:179], 1.0 op_sel_hi:[1,1,0]
	v_pk_fma_f32 v[186:187], v[182:183], v[176:177], 1.0 op_sel_hi:[1,1,0]
	v_pk_fma_f32 v[240:241], v[238:239], v[234:235], 1.0 op_sel_hi:[1,1,0]
	v_pk_fma_f32 v[242:243], v[238:239], v[232:233], 1.0 op_sel_hi:[1,1,0]
	v_cvt_pk_bf16_f32 v154, v138, v139
	v_cvt_pk_bf16_f32 v155, v140, v141
	v_cvt_pk_bf16_f32 v156, v150, v151
	v_cvt_pk_bf16_f32 v157, v152, v153
	v_cvt_pk_bf16_f32 v158, v184, v185
	v_cvt_pk_bf16_f32 v159, v186, v187
	v_cvt_pk_bf16_f32 v160, v240, v241
	v_cvt_pk_bf16_f32 v161, v242, v243
	ds_read_b128 v[114:117], v172
	ds_read_b128 v[78:81], v172 offset:64
	ds_read_b128 v[106:109], v172 offset:128
	ds_read_b128 v[70:73], v172 offset:192
	v_permlane16_swap_b32_e32 v154, v156
	v_permlane16_swap_b32_e32 v155, v157
	global_store_dwordx4 v228, v[154:157], s[58:59] nt
	s_bitcmp1_b32 s20, 12
	s_cbranch_scc1 .Lg1_noX
	s_barrier
.Lg1_noX:
	v_permlane16_swap_b32_e32 v158, v160
	v_permlane16_swap_b32_e32 v159, v161
	global_store_dwordx4 v228, v[158:161], s[58:59] offset:128 nt
	v_exp_f32_e32 v130, v90
	v_exp_f32_e32 v131, v91
	v_exp_f32_e32 v132, v92
	v_exp_f32_e32 v133, v93
	v_exp_f32_e32 v142, v42
	v_exp_f32_e32 v143, v43
	v_exp_f32_e32 v144, v44
	v_exp_f32_e32 v145, v45
	v_exp_f32_e32 v176, v126
	v_exp_f32_e32 v177, v127
	v_exp_f32_e32 v178, v128
	v_exp_f32_e32 v179, v129
	v_exp_f32_e32 v232, v58
	v_exp_f32_e32 v233, v59
	v_exp_f32_e32 v234, v60
	v_exp_f32_e32 v235, v61
	v_pk_fma_f32 v[130:131], v[130:131], -0.5, -0.5 op_sel_hi:[1,0,0]
	v_pk_fma_f32 v[132:133], v[132:133], -0.5, -0.5 op_sel_hi:[1,0,0]
	v_pk_fma_f32 v[142:143], v[142:143], -0.5, -0.5 op_sel_hi:[1,0,0]
	v_pk_fma_f32 v[144:145], v[144:145], -0.5, -0.5 op_sel_hi:[1,0,0]
	v_pk_fma_f32 v[176:177], v[176:177], -0.5, -0.5 op_sel_hi:[1,0,0]
	v_pk_fma_f32 v[178:179], v[178:179], -0.5, -0.5 op_sel_hi:[1,0,0]
	v_pk_fma_f32 v[232:233], v[232:233], -0.5, -0.5 op_sel_hi:[1,0,0]
	v_pk_fma_f32 v[234:235], v[234:235], -0.5, -0.5 op_sel_hi:[1,0,0]
	v_pk_mul_f32 v[134:135], v[130:131], v[132:133]
	v_pk_mul_f32 v[146:147], v[142:143], v[144:145]
	v_pk_mul_f32 v[180:181], v[176:177], v[178:179]
	v_pk_mul_f32 v[236:237], v[232:233], v[234:235]
	v_rcp_f32_e32 v136, v134
	v_rcp_f32_e32 v137, v135
	v_rcp_f32_e32 v148, v146
	v_rcp_f32_e32 v149, v147
	v_rcp_f32_e32 v182, v180
	v_rcp_f32_e32 v183, v181
	v_rcp_f32_e32 v238, v236
	v_rcp_f32_e32 v239, v237
	v_pk_add_f32 v[164:165], v[164:165], v[90:91]
	v_pk_add_f32 v[164:165], v[164:165], v[92:93]
	v_pk_add_f32 v[164:165], v[164:165], v[42:43]
	v_pk_add_f32 v[164:165], v[164:165], v[44:45]
	v_pk_add_f32 v[164:165], v[164:165], v[126:127]
	v_pk_add_f32 v[164:165], v[164:165], v[128:129]
	v_pk_add_f32 v[164:165], v[164:165], v[58:59]
	v_pk_add_f32 v[164:165], v[164:165], v[60:61]
	v_pk_mul_f32 v[174:175], v[134:135], v[146:147]
	v_pk_mul_f32 v[174:175], v[174:175], v[180:181]
	v_pk_mul_f32 v[174:175], v[174:175], v[236:237]
	v_pk_fma_f32 v[138:139], v[136:137], v[132:133], 1.0 op_sel_hi:[1,1,0]
	v_pk_fma_f32 v[140:141], v[136:137], v[130:131], 1.0 op_sel_hi:[1,1,0]
	v_pk_fma_f32 v[150:151], v[148:149], v[144:145], 1.0 op_sel_hi:[1,1,0]
	v_pk_fma_f32 v[152:153], v[148:149], v[142:143], 1.0 op_sel_hi:[1,1,0]
	v_pk_fma_f32 v[184:185], v[182:183], v[178:179], 1.0 op_sel_hi:[1,1,0]
	v_pk_fma_f32 v[186:187], v[182:183], v[176:177], 1.0 op_sel_hi:[1,1,0]
	v_pk_fma_f32 v[240:241], v[238:239], v[234:235], 1.0 op_sel_hi:[1,1,0]
	v_pk_fma_f32 v[242:243], v[238:239], v[232:233], 1.0 op_sel_hi:[1,1,0]
	v_cvt_pk_bf16_f32 v154, v138, v139
	v_cvt_pk_bf16_f32 v155, v140, v141
	v_cvt_pk_bf16_f32 v156, v150, v151
	v_cvt_pk_bf16_f32 v157, v152, v153
	v_cvt_pk_bf16_f32 v158, v184, v185
	v_cvt_pk_bf16_f32 v159, v186, v187
	v_cvt_pk_bf16_f32 v160, v240, v241
	v_cvt_pk_bf16_f32 v161, v242, v243
	ds_read_b128 v[90:93], v172 offset:512
	ds_read_b128 v[42:45], v172 offset:576
	ds_read_b128 v[126:129], v172 offset:640
	ds_read_b128 v[58:61], v172 offset:704
	v_permlane16_swap_b32_e32 v154, v156
	v_permlane16_swap_b32_e32 v155, v157
	global_store_dwordx4 v228, v[154:157], s[62:63] nt
	v_permlane16_swap_b32_e32 v158, v160
	v_permlane16_swap_b32_e32 v159, v161
	global_store_dwordx4 v228, v[158:161], s[62:63] offset:128 nt
	v_log_f32_e32 v166, v162
	v_log_f32_e32 v167, v163
	v_log_f32_e32 v170, v174
	v_log_f32_e32 v171, v175
	v_add_f32_e32 v168, v164, v165
	v_mul_f32_e32 v168, 0xbeb17218, v168
	v_add_f32_e32 v166, v166, v167
	v_add_f32_e32 v170, v170, v171
	v_add_f32_e32 v166, v166, v170
	v_fmac_f32_e32 v168, 0x3f317218, v166
	v_mov_b32_e32 v169, v168
	s_nop 1
	v_permlane16_swap_b32_e32 v168, v169
	v_add_f32_e32 v168, v168, v169
	v_mov_b32_e32 v169, v168
	s_nop 1
	v_permlane32_swap_b32_e32 v168, v169
	v_add_f32_e32 v168, v168, v169
	s_mov_b64 exec, s[0:1]
	global_store_dword v229, v168, s[66:67]
	s_mov_b64 exec, -1
	v_exp_f32_e32 v130, v110
	v_exp_f32_e32 v131, v111
	v_exp_f32_e32 v132, v112
	v_exp_f32_e32 v133, v113
	v_exp_f32_e32 v142, v74
	v_exp_f32_e32 v143, v75
	v_exp_f32_e32 v144, v76
	v_exp_f32_e32 v145, v77
	v_exp_f32_e32 v176, v102
	v_exp_f32_e32 v177, v103
	v_exp_f32_e32 v178, v104
	v_exp_f32_e32 v179, v105
	v_exp_f32_e32 v232, v66
	v_exp_f32_e32 v233, v67
	v_exp_f32_e32 v234, v68
	v_exp_f32_e32 v235, v69
	v_pk_fma_f32 v[130:131], v[130:131], -0.5, -0.5 op_sel_hi:[1,0,0]
	v_pk_fma_f32 v[132:133], v[132:133], -0.5, -0.5 op_sel_hi:[1,0,0]
	v_pk_fma_f32 v[142:143], v[142:143], -0.5, -0.5 op_sel_hi:[1,0,0]
	v_pk_fma_f32 v[144:145], v[144:145], -0.5, -0.5 op_sel_hi:[1,0,0]
	v_pk_fma_f32 v[176:177], v[176:177], -0.5, -0.5 op_sel_hi:[1,0,0]
	v_pk_fma_f32 v[178:179], v[178:179], -0.5, -0.5 op_sel_hi:[1,0,0]
	v_pk_fma_f32 v[232:233], v[232:233], -0.5, -0.5 op_sel_hi:[1,0,0]
	v_pk_fma_f32 v[234:235], v[234:235], -0.5, -0.5 op_sel_hi:[1,0,0]
	v_pk_mul_f32 v[134:135], v[130:131], v[132:133]
	v_pk_mul_f32 v[146:147], v[142:143], v[144:145]
	v_pk_mul_f32 v[180:181], v[176:177], v[178:179]
	v_pk_mul_f32 v[236:237], v[232:233], v[234:235]
	v_rcp_f32_e32 v136, v134
	v_rcp_f32_e32 v137, v135
	v_rcp_f32_e32 v148, v146
	v_rcp_f32_e32 v149, v147
	v_rcp_f32_e32 v182, v180
	v_rcp_f32_e32 v183, v181
	v_rcp_f32_e32 v238, v236
	v_rcp_f32_e32 v239, v237
	v_pk_add_f32 v[164:165], v[110:111], v[112:113]
	v_pk_add_f32 v[164:165], v[164:165], v[74:75]
	v_pk_add_f32 v[164:165], v[164:165], v[76:77]
	v_pk_add_f32 v[164:165], v[164:165], v[102:103]
	v_pk_add_f32 v[164:165], v[164:165], v[104:105]
	v_pk_add_f32 v[164:165], v[164:165], v[66:67]
	v_pk_add_f32 v[164:165], v[164:165], v[68:69]
	v_pk_mul_f32 v[162:163], v[134:135], v[146:147]
	v_pk_mul_f32 v[162:163], v[162:163], v[180:181]
	v_pk_mul_f32 v[162:163], v[162:163], v[236:237]
	v_pk_fma_f32 v[138:139], v[136:137], v[132:133], 1.0 op_sel_hi:[1,1,0]
	v_pk_fma_f32 v[140:141], v[136:137], v[130:131], 1.0 op_sel_hi:[1,1,0]
	v_pk_fma_f32 v[150:151], v[148:149], v[144:145], 1.0 op_sel_hi:[1,1,0]
	v_pk_fma_f32 v[152:153], v[148:149], v[142:143], 1.0 op_sel_hi:[1,1,0]
	v_pk_fma_f32 v[184:185], v[182:183], v[178:179], 1.0 op_sel_hi:[1,1,0]
	v_pk_fma_f32 v[186:187], v[182:183], v[176:177], 1.0 op_sel_hi:[1,1,0]
	v_pk_fma_f32 v[240:241], v[238:239], v[234:235], 1.0 op_sel_hi:[1,1,0]
	v_pk_fma_f32 v[242:243], v[238:239], v[232:233], 1.0 op_sel_hi:[1,1,0]
	v_cvt_pk_bf16_f32 v154, v138, v139
	v_cvt_pk_bf16_f32 v155, v140, v141
	v_cvt_pk_bf16_f32 v156, v150, v151
	v_cvt_pk_bf16_f32 v157, v152, v153
	v_cvt_pk_bf16_f32 v158, v184, v185
	v_cvt_pk_bf16_f32 v159, v186, v187
	v_cvt_pk_bf16_f32 v160, v240, v241
	v_cvt_pk_bf16_f32 v161, v242, v243
	ds_read_b128 v[110:113], v172
	ds_read_b128 v[74:77], v172 offset:64
	ds_read_b128 v[102:105], v172 offset:128
	ds_read_b128 v[66:69], v172 offset:192
	v_permlane16_swap_b32_e32 v154, v156
	v_permlane16_swap_b32_e32 v155, v157
	global_store_dwordx4 v228, v[154:157], s[58:59] offset:2048 nt
	v_permlane16_swap_b32_e32 v158, v160
	v_permlane16_swap_b32_e32 v159, v161
	global_store_dwordx4 v228, v[158:161], s[58:59] offset:2176 nt
	v_exp_f32_e32 v130, v86
	v_exp_f32_e32 v131, v87
	v_exp_f32_e32 v132, v88
	v_exp_f32_e32 v133, v89
	v_exp_f32_e32 v142, v38
	v_exp_f32_e32 v143, v39
	v_exp_f32_e32 v144, v40
	v_exp_f32_e32 v145, v41
	v_exp_f32_e32 v176, v122
	v_exp_f32_e32 v177, v123
	v_exp_f32_e32 v178, v124
	v_exp_f32_e32 v179, v125
	v_exp_f32_e32 v232, v50
	v_exp_f32_e32 v233, v51
	v_exp_f32_e32 v234, v52
	v_exp_f32_e32 v235, v53
	v_pk_fma_f32 v[130:131], v[130:131], -0.5, -0.5 op_sel_hi:[1,0,0]
	v_pk_fma_f32 v[132:133], v[132:133], -0.5, -0.5 op_sel_hi:[1,0,0]
	v_pk_fma_f32 v[142:143], v[142:143], -0.5, -0.5 op_sel_hi:[1,0,0]
	v_pk_fma_f32 v[144:145], v[144:145], -0.5, -0.5 op_sel_hi:[1,0,0]
	v_pk_fma_f32 v[176:177], v[176:177], -0.5, -0.5 op_sel_hi:[1,0,0]
	v_pk_fma_f32 v[178:179], v[178:179], -0.5, -0.5 op_sel_hi:[1,0,0]
	v_pk_fma_f32 v[232:233], v[232:233], -0.5, -0.5 op_sel_hi:[1,0,0]
	v_pk_fma_f32 v[234:235], v[234:235], -0.5, -0.5 op_sel_hi:[1,0,0]
	v_pk_mul_f32 v[134:135], v[130:131], v[132:133]
	v_pk_mul_f32 v[146:147], v[142:143], v[144:145]
	v_pk_mul_f32 v[180:181], v[176:177], v[178:179]
	v_pk_mul_f32 v[236:237], v[232:233], v[234:235]
	v_rcp_f32_e32 v136, v134
	v_rcp_f32_e32 v137, v135
	v_rcp_f32_e32 v148, v146
	v_rcp_f32_e32 v149, v147
	v_rcp_f32_e32 v182, v180
	v_rcp_f32_e32 v183, v181
	v_rcp_f32_e32 v238, v236
	v_rcp_f32_e32 v239, v237
	v_pk_add_f32 v[164:165], v[164:165], v[86:87]
	v_pk_add_f32 v[164:165], v[164:165], v[88:89]
	v_pk_add_f32 v[164:165], v[164:165], v[38:39]
	v_pk_add_f32 v[164:165], v[164:165], v[40:41]
	v_pk_add_f32 v[164:165], v[164:165], v[122:123]
	v_pk_add_f32 v[164:165], v[164:165], v[124:125]
	v_pk_add_f32 v[164:165], v[164:165], v[50:51]
	v_pk_add_f32 v[164:165], v[164:165], v[52:53]
	v_pk_mul_f32 v[174:175], v[134:135], v[146:147]
	v_pk_mul_f32 v[174:175], v[174:175], v[180:181]
	v_pk_mul_f32 v[174:175], v[174:175], v[236:237]
	v_pk_fma_f32 v[138:139], v[136:137], v[132:133], 1.0 op_sel_hi:[1,1,0]
	v_pk_fma_f32 v[140:141], v[136:137], v[130:131], 1.0 op_sel_hi:[1,1,0]
	v_pk_fma_f32 v[150:151], v[148:149], v[144:145], 1.0 op_sel_hi:[1,1,0]
	v_pk_fma_f32 v[152:153], v[148:149], v[142:143], 1.0 op_sel_hi:[1,1,0]
	v_pk_fma_f32 v[184:185], v[182:183], v[178:179], 1.0 op_sel_hi:[1,1,0]
	v_pk_fma_f32 v[186:187], v[182:183], v[176:177], 1.0 op_sel_hi:[1,1,0]
	v_pk_fma_f32 v[240:241], v[238:239], v[234:235], 1.0 op_sel_hi:[1,1,0]
	v_pk_fma_f32 v[242:243], v[238:239], v[232:233], 1.0 op_sel_hi:[1,1,0]
	v_cvt_pk_bf16_f32 v154, v138, v139
	v_cvt_pk_bf16_f32 v155, v140, v141
	v_cvt_pk_bf16_f32 v156, v150, v151
	v_cvt_pk_bf16_f32 v157, v152, v153
	v_cvt_pk_bf16_f32 v158, v184, v185
	v_cvt_pk_bf16_f32 v159, v186, v187
	v_cvt_pk_bf16_f32 v160, v240, v241
	v_cvt_pk_bf16_f32 v161, v242, v243
	ds_read_b128 v[86:89], v172 offset:512
	ds_read_b128 v[38:41], v172 offset:576
	ds_read_b128 v[122:125], v172 offset:640
	ds_read_b128 v[50:53], v172 offset:704
	v_permlane16_swap_b32_e32 v154, v156
	v_permlane16_swap_b32_e32 v155, v157
	global_store_dwordx4 v228, v[154:157], s[62:63] offset:2048 nt
	v_permlane16_swap_b32_e32 v158, v160
	v_permlane16_swap_b32_e32 v159, v161
	global_store_dwordx4 v228, v[158:161], s[62:63] offset:2176 nt
	v_log_f32_e32 v166, v162
	v_log_f32_e32 v167, v163
	v_log_f32_e32 v170, v174
	v_log_f32_e32 v171, v175
	v_add_f32_e32 v168, v164, v165
	v_mul_f32_e32 v168, 0xbeb17218, v168
	v_add_f32_e32 v166, v166, v167
	v_add_f32_e32 v170, v170, v171
	v_add_f32_e32 v166, v166, v170
	v_fmac_f32_e32 v168, 0x3f317218, v166
	v_mov_b32_e32 v169, v168
	s_nop 1
	v_permlane16_swap_b32_e32 v168, v169
	v_add_f32_e32 v168, v168, v169
	v_mov_b32_e32 v169, v168
	s_nop 1
	v_permlane32_swap_b32_e32 v168, v169
	v_add_f32_e32 v168, v168, v169
	s_mov_b64 exec, s[0:1]
	global_store_dword v229, v168, s[66:67] offset:64
	s_mov_b64 exec, -1
	v_exp_f32_e32 v130, v98
	v_exp_f32_e32 v131, v99
	v_exp_f32_e32 v132, v100
	v_exp_f32_e32 v133, v101
	v_exp_f32_e32 v142, v62
	v_exp_f32_e32 v143, v63
	v_exp_f32_e32 v144, v64
	v_exp_f32_e32 v145, v65
	v_exp_f32_e32 v176, v94
	v_exp_f32_e32 v177, v95
	v_exp_f32_e32 v178, v96
	v_exp_f32_e32 v179, v97
	v_exp_f32_e32 v232, v54
	v_exp_f32_e32 v233, v55
	v_exp_f32_e32 v234, v56
	v_exp_f32_e32 v235, v57
	v_pk_fma_f32 v[130:131], v[130:131], -0.5, -0.5 op_sel_hi:[1,0,0]
	v_pk_fma_f32 v[132:133], v[132:133], -0.5, -0.5 op_sel_hi:[1,0,0]
	v_pk_fma_f32 v[142:143], v[142:143], -0.5, -0.5 op_sel_hi:[1,0,0]
	v_pk_fma_f32 v[144:145], v[144:145], -0.5, -0.5 op_sel_hi:[1,0,0]
	v_pk_fma_f32 v[176:177], v[176:177], -0.5, -0.5 op_sel_hi:[1,0,0]
	v_pk_fma_f32 v[178:179], v[178:179], -0.5, -0.5 op_sel_hi:[1,0,0]
	v_pk_fma_f32 v[232:233], v[232:233], -0.5, -0.5 op_sel_hi:[1,0,0]
	v_pk_fma_f32 v[234:235], v[234:235], -0.5, -0.5 op_sel_hi:[1,0,0]
	v_pk_mul_f32 v[134:135], v[130:131], v[132:133]
	v_pk_mul_f32 v[146:147], v[142:143], v[144:145]
	v_pk_mul_f32 v[180:181], v[176:177], v[178:179]
	v_pk_mul_f32 v[236:237], v[232:233], v[234:235]
	v_rcp_f32_e32 v136, v134
	v_rcp_f32_e32 v137, v135
	v_rcp_f32_e32 v148, v146
	v_rcp_f32_e32 v149, v147
	v_rcp_f32_e32 v182, v180
	v_rcp_f32_e32 v183, v181
	v_rcp_f32_e32 v238, v236
	v_rcp_f32_e32 v239, v237
	v_pk_add_f32 v[164:165], v[98:99], v[100:101]
	v_pk_add_f32 v[164:165], v[164:165], v[62:63]
	v_pk_add_f32 v[164:165], v[164:165], v[64:65]
	v_pk_add_f32 v[164:165], v[164:165], v[94:95]
	v_pk_add_f32 v[164:165], v[164:165], v[96:97]
	v_pk_add_f32 v[164:165], v[164:165], v[54:55]
	v_pk_add_f32 v[164:165], v[164:165], v[56:57]
	v_pk_mul_f32 v[162:163], v[134:135], v[146:147]
	v_pk_mul_f32 v[162:163], v[162:163], v[180:181]
	v_pk_mul_f32 v[162:163], v[162:163], v[236:237]
	v_pk_fma_f32 v[138:139], v[136:137], v[132:133], 1.0 op_sel_hi:[1,1,0]
	v_pk_fma_f32 v[140:141], v[136:137], v[130:131], 1.0 op_sel_hi:[1,1,0]
	v_pk_fma_f32 v[150:151], v[148:149], v[144:145], 1.0 op_sel_hi:[1,1,0]
	v_pk_fma_f32 v[152:153], v[148:149], v[142:143], 1.0 op_sel_hi:[1,1,0]
	v_pk_fma_f32 v[184:185], v[182:183], v[178:179], 1.0 op_sel_hi:[1,1,0]
	v_pk_fma_f32 v[186:187], v[182:183], v[176:177], 1.0 op_sel_hi:[1,1,0]
	v_pk_fma_f32 v[240:241], v[238:239], v[234:235], 1.0 op_sel_hi:[1,1,0]
	v_pk_fma_f32 v[242:243], v[238:239], v[232:233], 1.0 op_sel_hi:[1,1,0]
	v_cvt_pk_bf16_f32 v154, v138, v139
	v_cvt_pk_bf16_f32 v155, v140, v141
	v_cvt_pk_bf16_f32 v156, v150, v151
	v_cvt_pk_bf16_f32 v157, v152, v153
	v_cvt_pk_bf16_f32 v158, v184, v185
	v_cvt_pk_bf16_f32 v159, v186, v187
	v_cvt_pk_bf16_f32 v160, v240, v241
	v_cvt_pk_bf16_f32 v161, v242, v243
	ds_read_b128 v[98:101], v172
	ds_read_b128 v[62:65], v172 offset:64
	ds_read_b128 v[94:97], v172 offset:128
	ds_read_b128 v[54:57], v172 offset:192
	v_permlane16_swap_b32_e32 v154, v156
	v_permlane16_swap_b32_e32 v155, v157
	global_store_dwordx4 v228, v[154:157], s[60:61] nt
	v_permlane16_swap_b32_e32 v158, v160
	v_permlane16_swap_b32_e32 v159, v161
	global_store_dwordx4 v228, v[158:161], s[60:61] offset:128 nt
	v_exp_f32_e32 v130, v82
	v_exp_f32_e32 v131, v83
	v_exp_f32_e32 v132, v84
	v_exp_f32_e32 v133, v85
	v_exp_f32_e32 v142, v34
	v_exp_f32_e32 v143, v35
	v_exp_f32_e32 v144, v36
	v_exp_f32_e32 v145, v37
	v_exp_f32_e32 v176, v118
	v_exp_f32_e32 v177, v119
	v_exp_f32_e32 v178, v120
	v_exp_f32_e32 v179, v121
	v_exp_f32_e32 v232, v46
	v_exp_f32_e32 v233, v47
	v_exp_f32_e32 v234, v48
	v_exp_f32_e32 v235, v49
	v_pk_fma_f32 v[130:131], v[130:131], -0.5, -0.5 op_sel_hi:[1,0,0]
	v_pk_fma_f32 v[132:133], v[132:133], -0.5, -0.5 op_sel_hi:[1,0,0]
	v_pk_fma_f32 v[142:143], v[142:143], -0.5, -0.5 op_sel_hi:[1,0,0]
	v_pk_fma_f32 v[144:145], v[144:145], -0.5, -0.5 op_sel_hi:[1,0,0]
	v_pk_fma_f32 v[176:177], v[176:177], -0.5, -0.5 op_sel_hi:[1,0,0]
	v_pk_fma_f32 v[178:179], v[178:179], -0.5, -0.5 op_sel_hi:[1,0,0]
	v_pk_fma_f32 v[232:233], v[232:233], -0.5, -0.5 op_sel_hi:[1,0,0]
	v_pk_fma_f32 v[234:235], v[234:235], -0.5, -0.5 op_sel_hi:[1,0,0]
	v_pk_mul_f32 v[134:135], v[130:131], v[132:133]
	v_pk_mul_f32 v[146:147], v[142:143], v[144:145]
	v_pk_mul_f32 v[180:181], v[176:177], v[178:179]
	v_pk_mul_f32 v[236:237], v[232:233], v[234:235]
	v_rcp_f32_e32 v136, v134
	v_rcp_f32_e32 v137, v135
	v_rcp_f32_e32 v148, v146
	v_rcp_f32_e32 v149, v147
	v_rcp_f32_e32 v182, v180
	v_rcp_f32_e32 v183, v181
	v_rcp_f32_e32 v238, v236
	v_rcp_f32_e32 v239, v237
	v_pk_add_f32 v[164:165], v[164:165], v[82:83]
	v_pk_add_f32 v[164:165], v[164:165], v[84:85]
	v_pk_add_f32 v[164:165], v[164:165], v[34:35]
	v_pk_add_f32 v[164:165], v[164:165], v[36:37]
	v_pk_add_f32 v[164:165], v[164:165], v[118:119]
	v_pk_add_f32 v[164:165], v[164:165], v[120:121]
	v_pk_add_f32 v[164:165], v[164:165], v[46:47]
	v_pk_add_f32 v[164:165], v[164:165], v[48:49]
	v_pk_mul_f32 v[174:175], v[134:135], v[146:147]
	v_pk_mul_f32 v[174:175], v[174:175], v[180:181]
	v_pk_mul_f32 v[174:175], v[174:175], v[236:237]
	v_pk_fma_f32 v[138:139], v[136:137], v[132:133], 1.0 op_sel_hi:[1,1,0]
	v_pk_fma_f32 v[140:141], v[136:137], v[130:131], 1.0 op_sel_hi:[1,1,0]
	v_pk_fma_f32 v[150:151], v[148:149], v[144:145], 1.0 op_sel_hi:[1,1,0]
	v_pk_fma_f32 v[152:153], v[148:149], v[142:143], 1.0 op_sel_hi:[1,1,0]
	v_pk_fma_f32 v[184:185], v[182:183], v[178:179], 1.0 op_sel_hi:[1,1,0]
	v_pk_fma_f32 v[186:187], v[182:183], v[176:177], 1.0 op_sel_hi:[1,1,0]
	v_pk_fma_f32 v[240:241], v[238:239], v[234:235], 1.0 op_sel_hi:[1,1,0]
	v_pk_fma_f32 v[242:243], v[238:239], v[232:233], 1.0 op_sel_hi:[1,1,0]
	v_cvt_pk_bf16_f32 v154, v138, v139
	v_cvt_pk_bf16_f32 v155, v140, v141
	v_cvt_pk_bf16_f32 v156, v150, v151
	v_cvt_pk_bf16_f32 v157, v152, v153
	v_cvt_pk_bf16_f32 v158, v184, v185
	v_cvt_pk_bf16_f32 v159, v186, v187
	v_cvt_pk_bf16_f32 v160, v240, v241
	v_cvt_pk_bf16_f32 v161, v242, v243
	ds_read_b128 v[82:85], v172 offset:512
	ds_read_b128 v[34:37], v172 offset:576
	ds_read_b128 v[118:121], v172 offset:640
	ds_read_b128 v[46:49], v172 offset:704
	v_permlane16_swap_b32_e32 v154, v156
	v_permlane16_swap_b32_e32 v155, v157
	global_store_dwordx4 v228, v[154:157], s[64:65] nt
	v_permlane16_swap_b32_e32 v158, v160
	v_permlane16_swap_b32_e32 v159, v161
	global_store_dwordx4 v228, v[158:161], s[64:65] offset:128 nt
	v_log_f32_e32 v166, v162
	v_log_f32_e32 v167, v163
	v_log_f32_e32 v170, v174
	v_log_f32_e32 v171, v175
	v_add_f32_e32 v168, v164, v165
	v_mul_f32_e32 v168, 0xbeb17218, v168
	v_add_f32_e32 v166, v166, v167
	v_add_f32_e32 v170, v170, v171
	v_add_f32_e32 v166, v166, v170
	v_fmac_f32_e32 v168, 0x3f317218, v166
	v_mov_b32_e32 v169, v168
	s_nop 1
	v_permlane16_swap_b32_e32 v168, v169
	v_add_f32_e32 v168, v168, v169
	v_mov_b32_e32 v169, v168
	s_nop 1
	v_permlane32_swap_b32_e32 v168, v169
	v_add_f32_e32 v168, v168, v169
	s_mov_b64 exec, s[0:1]
	global_store_dword v229, v168, s[66:67] offset:512
	s_mov_b64 exec, -1
	s_bitcmp1_b32 s20, 12
	s_cbranch_scc0 .Lg1_noY
	s_barrier
.Lg1_noY:
	v_exp_f32_e32 v130, v18
	v_exp_f32_e32 v131, v19
	v_exp_f32_e32 v132, v20
	v_exp_f32_e32 v133, v21
	v_exp_f32_e32 v142, v2
	v_exp_f32_e32 v143, v3
	v_exp_f32_e32 v144, v4
	v_exp_f32_e32 v145, v5
	v_exp_f32_e32 v176, v26
	v_exp_f32_e32 v177, v27
	v_exp_f32_e32 v178, v28
	v_exp_f32_e32 v179, v29
	v_exp_f32_e32 v232, v10
	v_exp_f32_e32 v233, v11
	v_exp_f32_e32 v234, v12
	v_exp_f32_e32 v235, v13
	v_pk_fma_f32 v[130:131], v[130:131], -0.5, -0.5 op_sel_hi:[1,0,0]
	v_pk_fma_f32 v[132:133], v[132:133], -0.5, -0.5 op_sel_hi:[1,0,0]
	v_pk_fma_f32 v[142:143], v[142:143], -0.5, -0.5 op_sel_hi:[1,0,0]
	v_pk_fma_f32 v[144:145], v[144:145], -0.5, -0.5 op_sel_hi:[1,0,0]
	v_pk_fma_f32 v[176:177], v[176:177], -0.5, -0.5 op_sel_hi:[1,0,0]
	v_pk_fma_f32 v[178:179], v[178:179], -0.5, -0.5 op_sel_hi:[1,0,0]
	v_pk_fma_f32 v[232:233], v[232:233], -0.5, -0.5 op_sel_hi:[1,0,0]
	v_pk_fma_f32 v[234:235], v[234:235], -0.5, -0.5 op_sel_hi:[1,0,0]
	v_pk_mul_f32 v[134:135], v[130:131], v[132:133]
	v_pk_mul_f32 v[146:147], v[142:143], v[144:145]
	v_pk_mul_f32 v[180:181], v[176:177], v[178:179]
	v_pk_mul_f32 v[236:237], v[232:233], v[234:235]
	v_rcp_f32_e32 v136, v134
	v_rcp_f32_e32 v137, v135
	v_rcp_f32_e32 v148, v146
	v_rcp_f32_e32 v149, v147
	v_rcp_f32_e32 v182, v180
	v_rcp_f32_e32 v183, v181
	v_rcp_f32_e32 v238, v236
	v_rcp_f32_e32 v239, v237
	v_pk_add_f32 v[164:165], v[18:19], v[20:21]
	v_pk_add_f32 v[164:165], v[164:165], v[2:3]
	v_pk_add_f32 v[164:165], v[164:165], v[4:5]
	v_pk_add_f32 v[164:165], v[164:165], v[26:27]
	v_pk_add_f32 v[164:165], v[164:165], v[28:29]
	v_pk_add_f32 v[164:165], v[164:165], v[10:11]
	v_pk_add_f32 v[164:165], v[164:165], v[12:13]
	v_pk_mul_f32 v[162:163], v[134:135], v[146:147]
	v_pk_mul_f32 v[162:163], v[162:163], v[180:181]
	v_pk_mul_f32 v[162:163], v[162:163], v[236:237]
	v_pk_fma_f32 v[138:139], v[136:137], v[132:133], 1.0 op_sel_hi:[1,1,0]
	v_pk_fma_f32 v[140:141], v[136:137], v[130:131], 1.0 op_sel_hi:[1,1,0]
	v_pk_fma_f32 v[150:151], v[148:149], v[144:145], 1.0 op_sel_hi:[1,1,0]
	v_pk_fma_f32 v[152:153], v[148:149], v[142:143], 1.0 op_sel_hi:[1,1,0]
	v_pk_fma_f32 v[184:185], v[182:183], v[178:179], 1.0 op_sel_hi:[1,1,0]
	v_pk_fma_f32 v[186:187], v[182:183], v[176:177], 1.0 op_sel_hi:[1,1,0]
	v_pk_fma_f32 v[240:241], v[238:239], v[234:235], 1.0 op_sel_hi:[1,1,0]
	v_pk_fma_f32 v[242:243], v[238:239], v[232:233], 1.0 op_sel_hi:[1,1,0]
	v_cvt_pk_bf16_f32 v154, v138, v139
	v_cvt_pk_bf16_f32 v155, v140, v141
	v_cvt_pk_bf16_f32 v156, v150, v151
	v_cvt_pk_bf16_f32 v157, v152, v153
	v_cvt_pk_bf16_f32 v158, v184, v185
	v_cvt_pk_bf16_f32 v159, v186, v187
	v_cvt_pk_bf16_f32 v160, v240, v241
	v_cvt_pk_bf16_f32 v161, v242, v243
	ds_read_b128 v[18:21], v172
	ds_read_b128 v[2:5], v172 offset:64
	ds_read_b128 v[26:29], v172 offset:128
	ds_read_b128 v[10:13], v172 offset:192
	v_permlane16_swap_b32_e32 v154, v156
	v_permlane16_swap_b32_e32 v155, v157
	global_store_dwordx4 v228, v[154:157], s[60:61] offset:2048 nt
	v_permlane16_swap_b32_e32 v158, v160
	v_permlane16_swap_b32_e32 v159, v161
	global_store_dwordx4 v228, v[158:161], s[60:61] offset:2176 nt
	v_exp_f32_e32 v130, v22
	v_exp_f32_e32 v131, v23
	v_exp_f32_e32 v132, v24
	v_exp_f32_e32 v133, v25
	v_exp_f32_e32 v142, v6
	v_exp_f32_e32 v143, v7
	v_exp_f32_e32 v144, v8
	v_exp_f32_e32 v145, v9
	v_exp_f32_e32 v176, v30
	v_exp_f32_e32 v177, v31
	v_exp_f32_e32 v178, v32
	v_exp_f32_e32 v179, v33
	v_exp_f32_e32 v232, v14
	v_exp_f32_e32 v233, v15
	v_exp_f32_e32 v234, v16
	v_exp_f32_e32 v235, v17
	v_pk_fma_f32 v[130:131], v[130:131], -0.5, -0.5 op_sel_hi:[1,0,0]
	v_pk_fma_f32 v[132:133], v[132:133], -0.5, -0.5 op_sel_hi:[1,0,0]
	v_pk_fma_f32 v[142:143], v[142:143], -0.5, -0.5 op_sel_hi:[1,0,0]
	v_pk_fma_f32 v[144:145], v[144:145], -0.5, -0.5 op_sel_hi:[1,0,0]
	v_pk_fma_f32 v[176:177], v[176:177], -0.5, -0.5 op_sel_hi:[1,0,0]
	v_pk_fma_f32 v[178:179], v[178:179], -0.5, -0.5 op_sel_hi:[1,0,0]
	v_pk_fma_f32 v[232:233], v[232:233], -0.5, -0.5 op_sel_hi:[1,0,0]
	v_pk_fma_f32 v[234:235], v[234:235], -0.5, -0.5 op_sel_hi:[1,0,0]
	v_pk_mul_f32 v[134:135], v[130:131], v[132:133]
	v_pk_mul_f32 v[146:147], v[142:143], v[144:145]
	v_pk_mul_f32 v[180:181], v[176:177], v[178:179]
	v_pk_mul_f32 v[236:237], v[232:233], v[234:235]
	v_rcp_f32_e32 v136, v134
	v_rcp_f32_e32 v137, v135
	v_rcp_f32_e32 v148, v146
	v_rcp_f32_e32 v149, v147
	v_rcp_f32_e32 v182, v180
	v_rcp_f32_e32 v183, v181
	v_rcp_f32_e32 v238, v236
	v_rcp_f32_e32 v239, v237
	v_pk_add_f32 v[164:165], v[164:165], v[22:23]
	v_pk_add_f32 v[164:165], v[164:165], v[24:25]
	v_pk_add_f32 v[164:165], v[164:165], v[6:7]
	v_pk_add_f32 v[164:165], v[164:165], v[8:9]
	v_pk_add_f32 v[164:165], v[164:165], v[30:31]
	v_pk_add_f32 v[164:165], v[164:165], v[32:33]
	v_pk_add_f32 v[164:165], v[164:165], v[14:15]
	v_pk_add_f32 v[164:165], v[164:165], v[16:17]
	v_pk_mul_f32 v[174:175], v[134:135], v[146:147]
	v_pk_mul_f32 v[174:175], v[174:175], v[180:181]
	v_pk_mul_f32 v[174:175], v[174:175], v[236:237]
	v_pk_fma_f32 v[138:139], v[136:137], v[132:133], 1.0 op_sel_hi:[1,1,0]
	v_pk_fma_f32 v[140:141], v[136:137], v[130:131], 1.0 op_sel_hi:[1,1,0]
	v_pk_fma_f32 v[150:151], v[148:149], v[144:145], 1.0 op_sel_hi:[1,1,0]
	v_pk_fma_f32 v[152:153], v[148:149], v[142:143], 1.0 op_sel_hi:[1,1,0]
	v_pk_fma_f32 v[184:185], v[182:183], v[178:179], 1.0 op_sel_hi:[1,1,0]
	v_pk_fma_f32 v[186:187], v[182:183], v[176:177], 1.0 op_sel_hi:[1,1,0]
	v_pk_fma_f32 v[240:241], v[238:239], v[234:235], 1.0 op_sel_hi:[1,1,0]
	v_pk_fma_f32 v[242:243], v[238:239], v[232:233], 1.0 op_sel_hi:[1,1,0]
	v_cvt_pk_bf16_f32 v154, v138, v139
	v_cvt_pk_bf16_f32 v155, v140, v141
	v_cvt_pk_bf16_f32 v156, v150, v151
	v_cvt_pk_bf16_f32 v157, v152, v153
	v_cvt_pk_bf16_f32 v158, v184, v185
	v_cvt_pk_bf16_f32 v159, v186, v187
	v_cvt_pk_bf16_f32 v160, v240, v241
	v_cvt_pk_bf16_f32 v161, v242, v243
	ds_read_b128 v[22:25], v172 offset:512
	ds_read_b128 v[6:9], v172 offset:576
	ds_read_b128 v[30:33], v172 offset:640
	ds_read_b128 v[14:17], v172 offset:704
	v_permlane16_swap_b32_e32 v154, v156
	v_permlane16_swap_b32_e32 v155, v157
	global_store_dwordx4 v228, v[154:157], s[64:65] offset:2048 nt
	v_permlane16_swap_b32_e32 v158, v160
	v_permlane16_swap_b32_e32 v159, v161
	global_store_dwordx4 v228, v[158:161], s[64:65] offset:2176 nt
	v_log_f32_e32 v166, v162
	v_log_f32_e32 v167, v163
	v_log_f32_e32 v170, v174
	v_log_f32_e32 v171, v175
	v_add_f32_e32 v168, v164, v165
	v_mul_f32_e32 v168, 0xbeb17218, v168
	v_add_f32_e32 v166, v166, v167
	v_add_f32_e32 v170, v170, v171
	v_add_f32_e32 v166, v166, v170
	v_fmac_f32_e32 v168, 0x3f317218, v166
	v_mov_b32_e32 v169, v168
	s_nop 1
	v_permlane16_swap_b32_e32 v168, v169
	v_add_f32_e32 v168, v168, v169
	v_mov_b32_e32 v169, v168
	s_nop 1
	v_permlane32_swap_b32_e32 v168, v169
	v_add_f32_e32 v168, v168, v169
	s_mov_b64 exec, s[0:1]
	global_store_dword v229, v168, s[66:67] offset:576
	s_mov_b64 exec, -1
	s_mov_b64 s[2:3], 0
	s_branch .LBB3_5
